# combo7 + phase 10 contiguous-span layout, two tokens in flight, non-temporal (nt) output stores
# baseline (speedup 1.0000x reference)
.LBB0_1219:
	s_cmp_lt_i32 s48, 11
	s_cselect_b64 s[6:7], -1, 0
	s_and_b64 s[4:5], s[6:7], s[4:5]
	s_andn2_b64 vcc, exec, s[4:5]
	s_cbranch_vccnz .LBB0_1225
	s_load_dwordx4 s[4:7], s[0:1], 0xa8
	v_and_b32_e32 v1, 63, v0
	v_lshrrev_b32_e32 v5, 6, v0
	s_lshl_b32 s13, s2, 3
	v_readfirstlane_b32 s12, v5
	v_lshlrev_b32_e32 v2, 2, v1
	v_lshlrev_b32_e32 v3, 3, v1
	v_lshlrev_b32_e32 v4, 4, v1
	s_add_i32 s12, s12, s13
	v_lshl_add_u32 v5, v1, 11, s12
	v_lshlrev_b32_e32 v5, 3, v5
	v_cmp_gt_u32_e32 vcc, 8, v1
	s_waitcnt lgkmcnt(0)
	s_add_u32 s8, s6, 0x33c0a000
	s_addc_u32 s9, s7, 0
	s_add_u32 s10, s6, 0x33c2a000
	s_addc_u32 s11, s7, 0
	s_add_u32 s48, s6, 0x4744a000
	s_addc_u32 s49, s7, 0
	s_add_u32 s60, s6, 0x2b80a000
	s_addc_u32 s61, s7, 0
	s_lshl_b32 s14, s12, 12
	s_add_u32 s62, s60, s14
	s_addc_u32 s63, s61, 0
	s_lshl_b32 s14, s12, 13
	s_add_u32 s64, s4, s14
	s_addc_u32 s65, s5, 0
	s_and_saveexec_b64 s[14:15], vcc
	global_load_dwordx2 v[6:7], v5, s[8:9]
	global_load_dwordx2 v[8:9], v5, s[10:11]
	s_waitcnt vmcnt(1)
	v_ashrrev_i32_e32 v10, 16, v6
	v_ashrrev_i32_e32 v11, 16, v7
	v_lshlrev_b32_e32 v10, 2, v10
	v_lshlrev_b32_e32 v11, 2, v11
	v_add_u32_e32 v10, 0x24140, v10
	v_add_u32_e32 v11, 0x24140, v11
	ds_read_b32 v10, v10
	ds_read_b32 v11, v11
	v_and_b32_e32 v6, 0xffff, v6
	v_and_b32_e32 v7, 0xffff, v7
	s_waitcnt lgkmcnt(0)
	v_lshl_add_u32 v6, v10, 8, v6
	v_lshl_add_u32 v7, v11, 8, v7
	s_waitcnt vmcnt(0)
	s_mov_b64 exec, s[14:15]
	s_nop 1
	v_readlane_b32 s16, v6, 0
	v_readlane_b32 s24, v7, 0
	v_readlane_b32 s32, v8, 0
	v_readlane_b32 s40, v9, 0
	v_readlane_b32 s17, v6, 1
	v_readlane_b32 s25, v7, 1
	v_readlane_b32 s33, v8, 1
	v_readlane_b32 s41, v9, 1
	v_readlane_b32 s18, v6, 2
	v_readlane_b32 s26, v7, 2
	v_readlane_b32 s34, v8, 2
	v_readlane_b32 s42, v9, 2
	v_readlane_b32 s19, v6, 3
	v_readlane_b32 s27, v7, 3
	v_readlane_b32 s35, v8, 3
	v_readlane_b32 s43, v9, 3
	v_readlane_b32 s20, v6, 4
	v_readlane_b32 s28, v7, 4
	v_readlane_b32 s36, v8, 4
	v_readlane_b32 s44, v9, 4
	v_readlane_b32 s21, v6, 5
	v_readlane_b32 s29, v7, 5
	v_readlane_b32 s37, v8, 5
	v_readlane_b32 s45, v9, 5
	v_readlane_b32 s22, v6, 6
	v_readlane_b32 s30, v7, 6
	v_readlane_b32 s38, v8, 6
	v_readlane_b32 s46, v9, 6
	v_readlane_b32 s23, v6, 7
	v_readlane_b32 s31, v7, 7
	v_readlane_b32 s39, v8, 7
	v_readlane_b32 s47, v9, 7
	s_nop 3
	s_lshl_b32 s50, s16, 11
	s_add_u32 s50, s48, s50
	s_addc_u32 s51, s49, 0
	s_lshl_b32 s52, s24, 11
	s_add_u32 s52, s48, s52
	s_addc_u32 s53, s49, 0
	s_mov_b64 s[54:55], s[62:63]
	global_load_dword v64, v2, s[50:51]
	global_load_dword v65, v2, s[50:51] offset:256
	global_load_dword v66, v2, s[50:51] offset:512
	global_load_dword v67, v2, s[50:51] offset:768
	global_load_dword v68, v2, s[50:51] offset:1024
	global_load_dword v69, v2, s[50:51] offset:1280
	global_load_dword v70, v2, s[50:51] offset:1536
	global_load_dword v71, v2, s[50:51] offset:1792
	global_load_dword v72, v2, s[52:53]
	global_load_dword v73, v2, s[52:53] offset:256
	global_load_dword v74, v2, s[52:53] offset:512
	global_load_dword v75, v2, s[52:53] offset:768
	global_load_dword v76, v2, s[52:53] offset:1024
	global_load_dword v77, v2, s[52:53] offset:1280
	global_load_dword v78, v2, s[52:53] offset:1536
	global_load_dword v79, v2, s[52:53] offset:1792
	global_load_dwordx2 v[80:81], v3, s[54:55]
	global_load_dwordx2 v[82:83], v3, s[54:55] offset:512
	global_load_dwordx2 v[84:85], v3, s[54:55] offset:1024
	global_load_dwordx2 v[86:87], v3, s[54:55] offset:1536
	global_load_dwordx2 v[88:89], v3, s[54:55] offset:2048
	global_load_dwordx2 v[90:91], v3, s[54:55] offset:2560
	global_load_dwordx2 v[92:93], v3, s[54:55] offset:3072
	global_load_dwordx2 v[94:95], v3, s[54:55] offset:3584
	s_lshl_b32 s50, s17, 11
	s_add_u32 s50, s48, s50
	s_addc_u32 s51, s49, 0
	s_lshl_b32 s52, s25, 11
	s_add_u32 s52, s48, s52
	s_addc_u32 s53, s49, 0
	s_add_u32 s54, s62, 0x800000
	s_addc_u32 s55, s63, 0
	global_load_dword v96, v2, s[50:51]
	global_load_dword v97, v2, s[50:51] offset:256
	global_load_dword v98, v2, s[50:51] offset:512
	global_load_dword v99, v2, s[50:51] offset:768
	global_load_dword v100, v2, s[50:51] offset:1024
	global_load_dword v101, v2, s[50:51] offset:1280
	global_load_dword v102, v2, s[50:51] offset:1536
	global_load_dword v103, v2, s[50:51] offset:1792
	global_load_dword v104, v2, s[52:53]
	global_load_dword v105, v2, s[52:53] offset:256
	global_load_dword v106, v2, s[52:53] offset:512
	global_load_dword v107, v2, s[52:53] offset:768
	global_load_dword v108, v2, s[52:53] offset:1024
	global_load_dword v109, v2, s[52:53] offset:1280
	global_load_dword v110, v2, s[52:53] offset:1536
	global_load_dword v111, v2, s[52:53] offset:1792
	global_load_dwordx2 v[112:113], v3, s[54:55]
	global_load_dwordx2 v[114:115], v3, s[54:55] offset:512
	global_load_dwordx2 v[116:117], v3, s[54:55] offset:1024
	global_load_dwordx2 v[118:119], v3, s[54:55] offset:1536
	global_load_dwordx2 v[120:121], v3, s[54:55] offset:2048
	global_load_dwordx2 v[122:123], v3, s[54:55] offset:2560
	global_load_dwordx2 v[124:125], v3, s[54:55] offset:3072
	global_load_dwordx2 v[126:127], v3, s[54:55] offset:3584
	s_waitcnt vmcnt(24)
	s_lshl_b32 s50, s18, 11
	s_add_u32 s50, s48, s50
	s_addc_u32 s51, s49, 0
	s_lshl_b32 s52, s26, 11
	s_add_u32 s52, s48, s52
	s_addc_u32 s53, s49, 0
	s_add_u32 s54, s62, 0x1000000
	s_addc_u32 s55, s63, 0
	global_load_dword v128, v2, s[50:51]
	global_load_dword v129, v2, s[50:51] offset:256
	global_load_dword v130, v2, s[50:51] offset:512
	global_load_dword v131, v2, s[50:51] offset:768
	global_load_dword v132, v2, s[50:51] offset:1024
	global_load_dword v133, v2, s[50:51] offset:1280
	global_load_dword v134, v2, s[50:51] offset:1536
	global_load_dword v135, v2, s[50:51] offset:1792
	global_load_dword v136, v2, s[52:53]
	global_load_dword v137, v2, s[52:53] offset:256
	global_load_dword v138, v2, s[52:53] offset:512
	global_load_dword v139, v2, s[52:53] offset:768
	global_load_dword v140, v2, s[52:53] offset:1024
	global_load_dword v141, v2, s[52:53] offset:1280
	global_load_dword v142, v2, s[52:53] offset:1536
	global_load_dword v143, v2, s[52:53] offset:1792
	global_load_dwordx2 v[144:145], v3, s[54:55]
	global_load_dwordx2 v[146:147], v3, s[54:55] offset:512
	global_load_dwordx2 v[148:149], v3, s[54:55] offset:1024
	global_load_dwordx2 v[150:151], v3, s[54:55] offset:1536
	global_load_dwordx2 v[152:153], v3, s[54:55] offset:2048
	global_load_dwordx2 v[154:155], v3, s[54:55] offset:2560
	global_load_dwordx2 v[156:157], v3, s[54:55] offset:3072
	global_load_dwordx2 v[158:159], v3, s[54:55] offset:3584
	v_mov_b32_e32 v240, s32
	v_mov_b32_e32 v242, s40
	v_cvt_pk_f32_fp8_e32 v[224:225], v64
	v_cvt_pk_f32_fp8_sdwa v[226:227], v64 src0_sel:WORD_1
	v_cvt_pk_f32_fp8_e32 v[228:229], v72
	v_cvt_pk_f32_fp8_sdwa v[230:231], v72 src0_sel:WORD_1
	v_lshlrev_b32_e32 v192, 16, v80
	v_and_b32_e32 v193, 0xffff0000, v80
	v_lshlrev_b32_e32 v194, 16, v81
	v_and_b32_e32 v195, 0xffff0000, v81
	v_pk_fma_f32 v[192:193], v[224:225], v[240:241], v[192:193] op_sel_hi:[1,0,1]
	v_pk_fma_f32 v[194:195], v[226:227], v[240:241], v[194:195] op_sel_hi:[1,0,1]
	v_pk_fma_f32 v[192:193], v[228:229], v[242:243], v[192:193] op_sel_hi:[1,0,1]
	v_pk_fma_f32 v[194:195], v[230:231], v[242:243], v[194:195] op_sel_hi:[1,0,1]
	v_cvt_pk_f32_fp8_e32 v[232:233], v65
	v_cvt_pk_f32_fp8_sdwa v[234:235], v65 src0_sel:WORD_1
	v_cvt_pk_f32_fp8_e32 v[236:237], v73
	v_cvt_pk_f32_fp8_sdwa v[238:239], v73 src0_sel:WORD_1
	v_lshlrev_b32_e32 v196, 16, v82
	v_and_b32_e32 v197, 0xffff0000, v82
	v_lshlrev_b32_e32 v198, 16, v83
	v_and_b32_e32 v199, 0xffff0000, v83
	v_pk_fma_f32 v[196:197], v[232:233], v[240:241], v[196:197] op_sel_hi:[1,0,1]
	v_pk_fma_f32 v[198:199], v[234:235], v[240:241], v[198:199] op_sel_hi:[1,0,1]
	v_pk_fma_f32 v[196:197], v[236:237], v[242:243], v[196:197] op_sel_hi:[1,0,1]
	v_pk_fma_f32 v[198:199], v[238:239], v[242:243], v[198:199] op_sel_hi:[1,0,1]
	v_cvt_pk_f32_fp8_e32 v[224:225], v66
	v_cvt_pk_f32_fp8_sdwa v[226:227], v66 src0_sel:WORD_1
	v_cvt_pk_f32_fp8_e32 v[228:229], v74
	v_cvt_pk_f32_fp8_sdwa v[230:231], v74 src0_sel:WORD_1
	v_lshlrev_b32_e32 v200, 16, v84
	v_and_b32_e32 v201, 0xffff0000, v84
	v_lshlrev_b32_e32 v202, 16, v85
	v_and_b32_e32 v203, 0xffff0000, v85
	v_pk_fma_f32 v[200:201], v[224:225], v[240:241], v[200:201] op_sel_hi:[1,0,1]
	v_pk_fma_f32 v[202:203], v[226:227], v[240:241], v[202:203] op_sel_hi:[1,0,1]
	v_pk_fma_f32 v[200:201], v[228:229], v[242:243], v[200:201] op_sel_hi:[1,0,1]
	v_pk_fma_f32 v[202:203], v[230:231], v[242:243], v[202:203] op_sel_hi:[1,0,1]
	v_cvt_pk_f32_fp8_e32 v[232:233], v67
	v_cvt_pk_f32_fp8_sdwa v[234:235], v67 src0_sel:WORD_1
	v_cvt_pk_f32_fp8_e32 v[236:237], v75
	v_cvt_pk_f32_fp8_sdwa v[238:239], v75 src0_sel:WORD_1
	v_lshlrev_b32_e32 v204, 16, v86
	v_and_b32_e32 v205, 0xffff0000, v86
	v_lshlrev_b32_e32 v206, 16, v87
	v_and_b32_e32 v207, 0xffff0000, v87
	v_pk_fma_f32 v[204:205], v[232:233], v[240:241], v[204:205] op_sel_hi:[1,0,1]
	v_pk_fma_f32 v[206:207], v[234:235], v[240:241], v[206:207] op_sel_hi:[1,0,1]
	v_pk_fma_f32 v[204:205], v[236:237], v[242:243], v[204:205] op_sel_hi:[1,0,1]
	v_pk_fma_f32 v[206:207], v[238:239], v[242:243], v[206:207] op_sel_hi:[1,0,1]
	v_cvt_pk_f32_fp8_e32 v[224:225], v68
	v_cvt_pk_f32_fp8_sdwa v[226:227], v68 src0_sel:WORD_1
	v_cvt_pk_f32_fp8_e32 v[228:229], v76
	v_cvt_pk_f32_fp8_sdwa v[230:231], v76 src0_sel:WORD_1
	v_lshlrev_b32_e32 v208, 16, v88
	v_and_b32_e32 v209, 0xffff0000, v88
	v_lshlrev_b32_e32 v210, 16, v89
	v_and_b32_e32 v211, 0xffff0000, v89
	v_pk_fma_f32 v[208:209], v[224:225], v[240:241], v[208:209] op_sel_hi:[1,0,1]
	v_pk_fma_f32 v[210:211], v[226:227], v[240:241], v[210:211] op_sel_hi:[1,0,1]
	v_pk_fma_f32 v[208:209], v[228:229], v[242:243], v[208:209] op_sel_hi:[1,0,1]
	v_pk_fma_f32 v[210:211], v[230:231], v[242:243], v[210:211] op_sel_hi:[1,0,1]
	v_cvt_pk_f32_fp8_e32 v[232:233], v69
	v_cvt_pk_f32_fp8_sdwa v[234:235], v69 src0_sel:WORD_1
	v_cvt_pk_f32_fp8_e32 v[236:237], v77
	v_cvt_pk_f32_fp8_sdwa v[238:239], v77 src0_sel:WORD_1
	v_lshlrev_b32_e32 v212, 16, v90
	v_and_b32_e32 v213, 0xffff0000, v90
	v_lshlrev_b32_e32 v214, 16, v91
	v_and_b32_e32 v215, 0xffff0000, v91
	v_pk_fma_f32 v[212:213], v[232:233], v[240:241], v[212:213] op_sel_hi:[1,0,1]
	v_pk_fma_f32 v[214:215], v[234:235], v[240:241], v[214:215] op_sel_hi:[1,0,1]
	v_pk_fma_f32 v[212:213], v[236:237], v[242:243], v[212:213] op_sel_hi:[1,0,1]
	v_pk_fma_f32 v[214:215], v[238:239], v[242:243], v[214:215] op_sel_hi:[1,0,1]
	v_cvt_pk_f32_fp8_e32 v[224:225], v70
	v_cvt_pk_f32_fp8_sdwa v[226:227], v70 src0_sel:WORD_1
	v_cvt_pk_f32_fp8_e32 v[228:229], v78
	v_cvt_pk_f32_fp8_sdwa v[230:231], v78 src0_sel:WORD_1
	v_lshlrev_b32_e32 v216, 16, v92
	v_and_b32_e32 v217, 0xffff0000, v92
	v_lshlrev_b32_e32 v218, 16, v93
	v_and_b32_e32 v219, 0xffff0000, v93
	v_pk_fma_f32 v[216:217], v[224:225], v[240:241], v[216:217] op_sel_hi:[1,0,1]
	v_pk_fma_f32 v[218:219], v[226:227], v[240:241], v[218:219] op_sel_hi:[1,0,1]
	v_pk_fma_f32 v[216:217], v[228:229], v[242:243], v[216:217] op_sel_hi:[1,0,1]
	v_pk_fma_f32 v[218:219], v[230:231], v[242:243], v[218:219] op_sel_hi:[1,0,1]
	v_cvt_pk_f32_fp8_e32 v[232:233], v71
	v_cvt_pk_f32_fp8_sdwa v[234:235], v71 src0_sel:WORD_1
	v_cvt_pk_f32_fp8_e32 v[236:237], v79
	v_cvt_pk_f32_fp8_sdwa v[238:239], v79 src0_sel:WORD_1
	v_lshlrev_b32_e32 v220, 16, v94
	v_and_b32_e32 v221, 0xffff0000, v94
	v_lshlrev_b32_e32 v222, 16, v95
	v_and_b32_e32 v223, 0xffff0000, v95
	v_pk_fma_f32 v[220:221], v[232:233], v[240:241], v[220:221] op_sel_hi:[1,0,1]
	v_pk_fma_f32 v[222:223], v[234:235], v[240:241], v[222:223] op_sel_hi:[1,0,1]
	v_pk_fma_f32 v[220:221], v[236:237], v[242:243], v[220:221] op_sel_hi:[1,0,1]
	v_pk_fma_f32 v[222:223], v[238:239], v[242:243], v[222:223] op_sel_hi:[1,0,1]
	s_waitcnt vmcnt(55)
	s_mov_b64 s[56:57], s[64:65]
	s_add_u32 s58, s56, 0x1000
	s_addc_u32 s59, s57, 0
	global_store_dwordx4 v4, v[192:195], s[56:57] nt
	global_store_dwordx4 v4, v[196:199], s[56:57] offset:1024 nt
	global_store_dwordx4 v4, v[200:203], s[56:57] offset:2048 nt
	global_store_dwordx4 v4, v[204:207], s[56:57] offset:3072 nt
	global_store_dwordx4 v4, v[208:211], s[58:59] nt
	global_store_dwordx4 v4, v[212:215], s[58:59] offset:1024 nt
	global_store_dwordx4 v4, v[216:219], s[58:59] offset:2048 nt
	global_store_dwordx4 v4, v[220:223], s[58:59] offset:3072 nt
	s_waitcnt vmcnt(32)
	s_lshl_b32 s50, s19, 11
	s_add_u32 s50, s48, s50
	s_addc_u32 s51, s49, 0
	s_lshl_b32 s52, s27, 11
	s_add_u32 s52, s48, s52
	s_addc_u32 s53, s49, 0
	s_add_u32 s54, s62, 0x1800000
	s_addc_u32 s55, s63, 0
	global_load_dword v64, v2, s[50:51]
	global_load_dword v65, v2, s[50:51] offset:256
	global_load_dword v66, v2, s[50:51] offset:512
	global_load_dword v67, v2, s[50:51] offset:768
	global_load_dword v68, v2, s[50:51] offset:1024
	global_load_dword v69, v2, s[50:51] offset:1280
	global_load_dword v70, v2, s[50:51] offset:1536
	global_load_dword v71, v2, s[50:51] offset:1792
	global_load_dword v72, v2, s[52:53]
	global_load_dword v73, v2, s[52:53] offset:256
	global_load_dword v74, v2, s[52:53] offset:512
	global_load_dword v75, v2, s[52:53] offset:768
	global_load_dword v76, v2, s[52:53] offset:1024
	global_load_dword v77, v2, s[52:53] offset:1280
	global_load_dword v78, v2, s[52:53] offset:1536
	global_load_dword v79, v2, s[52:53] offset:1792
	global_load_dwordx2 v[80:81], v3, s[54:55]
	global_load_dwordx2 v[82:83], v3, s[54:55] offset:512
	global_load_dwordx2 v[84:85], v3, s[54:55] offset:1024
	global_load_dwordx2 v[86:87], v3, s[54:55] offset:1536
	global_load_dwordx2 v[88:89], v3, s[54:55] offset:2048
	global_load_dwordx2 v[90:91], v3, s[54:55] offset:2560
	global_load_dwordx2 v[92:93], v3, s[54:55] offset:3072
	global_load_dwordx2 v[94:95], v3, s[54:55] offset:3584
	v_mov_b32_e32 v240, s33
	v_mov_b32_e32 v242, s41
	v_cvt_pk_f32_fp8_e32 v[224:225], v96
	v_cvt_pk_f32_fp8_sdwa v[226:227], v96 src0_sel:WORD_1
	v_cvt_pk_f32_fp8_e32 v[228:229], v104
	v_cvt_pk_f32_fp8_sdwa v[230:231], v104 src0_sel:WORD_1
	v_lshlrev_b32_e32 v192, 16, v112
	v_and_b32_e32 v193, 0xffff0000, v112
	v_lshlrev_b32_e32 v194, 16, v113
	v_and_b32_e32 v195, 0xffff0000, v113
	v_pk_fma_f32 v[192:193], v[224:225], v[240:241], v[192:193] op_sel_hi:[1,0,1]
	v_pk_fma_f32 v[194:195], v[226:227], v[240:241], v[194:195] op_sel_hi:[1,0,1]
	v_pk_fma_f32 v[192:193], v[228:229], v[242:243], v[192:193] op_sel_hi:[1,0,1]
	v_pk_fma_f32 v[194:195], v[230:231], v[242:243], v[194:195] op_sel_hi:[1,0,1]
	v_cvt_pk_f32_fp8_e32 v[232:233], v97
	v_cvt_pk_f32_fp8_sdwa v[234:235], v97 src0_sel:WORD_1
	v_cvt_pk_f32_fp8_e32 v[236:237], v105
	v_cvt_pk_f32_fp8_sdwa v[238:239], v105 src0_sel:WORD_1
	v_lshlrev_b32_e32 v196, 16, v114
	v_and_b32_e32 v197, 0xffff0000, v114
	v_lshlrev_b32_e32 v198, 16, v115
	v_and_b32_e32 v199, 0xffff0000, v115
	v_pk_fma_f32 v[196:197], v[232:233], v[240:241], v[196:197] op_sel_hi:[1,0,1]
	v_pk_fma_f32 v[198:199], v[234:235], v[240:241], v[198:199] op_sel_hi:[1,0,1]
	v_pk_fma_f32 v[196:197], v[236:237], v[242:243], v[196:197] op_sel_hi:[1,0,1]
	v_pk_fma_f32 v[198:199], v[238:239], v[242:243], v[198:199] op_sel_hi:[1,0,1]
	v_cvt_pk_f32_fp8_e32 v[224:225], v98
	v_cvt_pk_f32_fp8_sdwa v[226:227], v98 src0_sel:WORD_1
	v_cvt_pk_f32_fp8_e32 v[228:229], v106
	v_cvt_pk_f32_fp8_sdwa v[230:231], v106 src0_sel:WORD_1
	v_lshlrev_b32_e32 v200, 16, v116
	v_and_b32_e32 v201, 0xffff0000, v116
	v_lshlrev_b32_e32 v202, 16, v117
	v_and_b32_e32 v203, 0xffff0000, v117
	v_pk_fma_f32 v[200:201], v[224:225], v[240:241], v[200:201] op_sel_hi:[1,0,1]
	v_pk_fma_f32 v[202:203], v[226:227], v[240:241], v[202:203] op_sel_hi:[1,0,1]
	v_pk_fma_f32 v[200:201], v[228:229], v[242:243], v[200:201] op_sel_hi:[1,0,1]
	v_pk_fma_f32 v[202:203], v[230:231], v[242:243], v[202:203] op_sel_hi:[1,0,1]
	v_cvt_pk_f32_fp8_e32 v[232:233], v99
	v_cvt_pk_f32_fp8_sdwa v[234:235], v99 src0_sel:WORD_1
	v_cvt_pk_f32_fp8_e32 v[236:237], v107
	v_cvt_pk_f32_fp8_sdwa v[238:239], v107 src0_sel:WORD_1
	v_lshlrev_b32_e32 v204, 16, v118
	v_and_b32_e32 v205, 0xffff0000, v118
	v_lshlrev_b32_e32 v206, 16, v119
	v_and_b32_e32 v207, 0xffff0000, v119
	v_pk_fma_f32 v[204:205], v[232:233], v[240:241], v[204:205] op_sel_hi:[1,0,1]
	v_pk_fma_f32 v[206:207], v[234:235], v[240:241], v[206:207] op_sel_hi:[1,0,1]
	v_pk_fma_f32 v[204:205], v[236:237], v[242:243], v[204:205] op_sel_hi:[1,0,1]
	v_pk_fma_f32 v[206:207], v[238:239], v[242:243], v[206:207] op_sel_hi:[1,0,1]
	v_cvt_pk_f32_fp8_e32 v[224:225], v100
	v_cvt_pk_f32_fp8_sdwa v[226:227], v100 src0_sel:WORD_1
	v_cvt_pk_f32_fp8_e32 v[228:229], v108
	v_cvt_pk_f32_fp8_sdwa v[230:231], v108 src0_sel:WORD_1
	v_lshlrev_b32_e32 v208, 16, v120
	v_and_b32_e32 v209, 0xffff0000, v120
	v_lshlrev_b32_e32 v210, 16, v121
	v_and_b32_e32 v211, 0xffff0000, v121
	v_pk_fma_f32 v[208:209], v[224:225], v[240:241], v[208:209] op_sel_hi:[1,0,1]
	v_pk_fma_f32 v[210:211], v[226:227], v[240:241], v[210:211] op_sel_hi:[1,0,1]
	v_pk_fma_f32 v[208:209], v[228:229], v[242:243], v[208:209] op_sel_hi:[1,0,1]
	v_pk_fma_f32 v[210:211], v[230:231], v[242:243], v[210:211] op_sel_hi:[1,0,1]
	v_cvt_pk_f32_fp8_e32 v[232:233], v101
	v_cvt_pk_f32_fp8_sdwa v[234:235], v101 src0_sel:WORD_1
	v_cvt_pk_f32_fp8_e32 v[236:237], v109
	v_cvt_pk_f32_fp8_sdwa v[238:239], v109 src0_sel:WORD_1
	v_lshlrev_b32_e32 v212, 16, v122
	v_and_b32_e32 v213, 0xffff0000, v122
	v_lshlrev_b32_e32 v214, 16, v123
	v_and_b32_e32 v215, 0xffff0000, v123
	v_pk_fma_f32 v[212:213], v[232:233], v[240:241], v[212:213] op_sel_hi:[1,0,1]
	v_pk_fma_f32 v[214:215], v[234:235], v[240:241], v[214:215] op_sel_hi:[1,0,1]
	v_pk_fma_f32 v[212:213], v[236:237], v[242:243], v[212:213] op_sel_hi:[1,0,1]
	v_pk_fma_f32 v[214:215], v[238:239], v[242:243], v[214:215] op_sel_hi:[1,0,1]
	v_cvt_pk_f32_fp8_e32 v[224:225], v102
	v_cvt_pk_f32_fp8_sdwa v[226:227], v102 src0_sel:WORD_1
	v_cvt_pk_f32_fp8_e32 v[228:229], v110
	v_cvt_pk_f32_fp8_sdwa v[230:231], v110 src0_sel:WORD_1
	v_lshlrev_b32_e32 v216, 16, v124
	v_and_b32_e32 v217, 0xffff0000, v124
	v_lshlrev_b32_e32 v218, 16, v125
	v_and_b32_e32 v219, 0xffff0000, v125
	v_pk_fma_f32 v[216:217], v[224:225], v[240:241], v[216:217] op_sel_hi:[1,0,1]
	v_pk_fma_f32 v[218:219], v[226:227], v[240:241], v[218:219] op_sel_hi:[1,0,1]
	v_pk_fma_f32 v[216:217], v[228:229], v[242:243], v[216:217] op_sel_hi:[1,0,1]
	v_pk_fma_f32 v[218:219], v[230:231], v[242:243], v[218:219] op_sel_hi:[1,0,1]
	v_cvt_pk_f32_fp8_e32 v[232:233], v103
	v_cvt_pk_f32_fp8_sdwa v[234:235], v103 src0_sel:WORD_1
	v_cvt_pk_f32_fp8_e32 v[236:237], v111
	v_cvt_pk_f32_fp8_sdwa v[238:239], v111 src0_sel:WORD_1
	v_lshlrev_b32_e32 v220, 16, v126
	v_and_b32_e32 v221, 0xffff0000, v126
	v_lshlrev_b32_e32 v222, 16, v127
	v_and_b32_e32 v223, 0xffff0000, v127
	v_pk_fma_f32 v[220:221], v[232:233], v[240:241], v[220:221] op_sel_hi:[1,0,1]
	v_pk_fma_f32 v[222:223], v[234:235], v[240:241], v[222:223] op_sel_hi:[1,0,1]
	v_pk_fma_f32 v[220:221], v[236:237], v[242:243], v[220:221] op_sel_hi:[1,0,1]
	v_pk_fma_f32 v[222:223], v[238:239], v[242:243], v[222:223] op_sel_hi:[1,0,1]
	s_waitcnt vmcnt(55)
	s_add_u32 s56, s64, 0x1000000
	s_addc_u32 s57, s65, 0
	s_add_u32 s58, s56, 0x1000
	s_addc_u32 s59, s57, 0
	global_store_dwordx4 v4, v[192:195], s[56:57] nt
	global_store_dwordx4 v4, v[196:199], s[56:57] offset:1024 nt
	global_store_dwordx4 v4, v[200:203], s[56:57] offset:2048 nt
	global_store_dwordx4 v4, v[204:207], s[56:57] offset:3072 nt
	global_store_dwordx4 v4, v[208:211], s[58:59] nt
	global_store_dwordx4 v4, v[212:215], s[58:59] offset:1024 nt
	global_store_dwordx4 v4, v[216:219], s[58:59] offset:2048 nt
	global_store_dwordx4 v4, v[220:223], s[58:59] offset:3072 nt
	s_waitcnt vmcnt(32)
	s_lshl_b32 s50, s20, 11
	s_add_u32 s50, s48, s50
	s_addc_u32 s51, s49, 0
	s_lshl_b32 s52, s28, 11
	s_add_u32 s52, s48, s52
	s_addc_u32 s53, s49, 0
	s_add_u32 s54, s62, 0x2000000
	s_addc_u32 s55, s63, 0
	global_load_dword v96, v2, s[50:51]
	global_load_dword v97, v2, s[50:51] offset:256
	global_load_dword v98, v2, s[50:51] offset:512
	global_load_dword v99, v2, s[50:51] offset:768
	global_load_dword v100, v2, s[50:51] offset:1024
	global_load_dword v101, v2, s[50:51] offset:1280
	global_load_dword v102, v2, s[50:51] offset:1536
	global_load_dword v103, v2, s[50:51] offset:1792
	global_load_dword v104, v2, s[52:53]
	global_load_dword v105, v2, s[52:53] offset:256
	global_load_dword v106, v2, s[52:53] offset:512
	global_load_dword v107, v2, s[52:53] offset:768
	global_load_dword v108, v2, s[52:53] offset:1024
	global_load_dword v109, v2, s[52:53] offset:1280
	global_load_dword v110, v2, s[52:53] offset:1536
	global_load_dword v111, v2, s[52:53] offset:1792
	global_load_dwordx2 v[112:113], v3, s[54:55]
	global_load_dwordx2 v[114:115], v3, s[54:55] offset:512
	global_load_dwordx2 v[116:117], v3, s[54:55] offset:1024
	global_load_dwordx2 v[118:119], v3, s[54:55] offset:1536
	global_load_dwordx2 v[120:121], v3, s[54:55] offset:2048
	global_load_dwordx2 v[122:123], v3, s[54:55] offset:2560
	global_load_dwordx2 v[124:125], v3, s[54:55] offset:3072
	global_load_dwordx2 v[126:127], v3, s[54:55] offset:3584
	v_mov_b32_e32 v240, s34
	v_mov_b32_e32 v242, s42
	v_cvt_pk_f32_fp8_e32 v[224:225], v128
	v_cvt_pk_f32_fp8_sdwa v[226:227], v128 src0_sel:WORD_1
	v_cvt_pk_f32_fp8_e32 v[228:229], v136
	v_cvt_pk_f32_fp8_sdwa v[230:231], v136 src0_sel:WORD_1
	v_lshlrev_b32_e32 v192, 16, v144
	v_and_b32_e32 v193, 0xffff0000, v144
	v_lshlrev_b32_e32 v194, 16, v145
	v_and_b32_e32 v195, 0xffff0000, v145
	v_pk_fma_f32 v[192:193], v[224:225], v[240:241], v[192:193] op_sel_hi:[1,0,1]
	v_pk_fma_f32 v[194:195], v[226:227], v[240:241], v[194:195] op_sel_hi:[1,0,1]
	v_pk_fma_f32 v[192:193], v[228:229], v[242:243], v[192:193] op_sel_hi:[1,0,1]
	v_pk_fma_f32 v[194:195], v[230:231], v[242:243], v[194:195] op_sel_hi:[1,0,1]
	v_cvt_pk_f32_fp8_e32 v[232:233], v129
	v_cvt_pk_f32_fp8_sdwa v[234:235], v129 src0_sel:WORD_1
	v_cvt_pk_f32_fp8_e32 v[236:237], v137
	v_cvt_pk_f32_fp8_sdwa v[238:239], v137 src0_sel:WORD_1
	v_lshlrev_b32_e32 v196, 16, v146
	v_and_b32_e32 v197, 0xffff0000, v146
	v_lshlrev_b32_e32 v198, 16, v147
	v_and_b32_e32 v199, 0xffff0000, v147
	v_pk_fma_f32 v[196:197], v[232:233], v[240:241], v[196:197] op_sel_hi:[1,0,1]
	v_pk_fma_f32 v[198:199], v[234:235], v[240:241], v[198:199] op_sel_hi:[1,0,1]
	v_pk_fma_f32 v[196:197], v[236:237], v[242:243], v[196:197] op_sel_hi:[1,0,1]
	v_pk_fma_f32 v[198:199], v[238:239], v[242:243], v[198:199] op_sel_hi:[1,0,1]
	v_cvt_pk_f32_fp8_e32 v[224:225], v130
	v_cvt_pk_f32_fp8_sdwa v[226:227], v130 src0_sel:WORD_1
	v_cvt_pk_f32_fp8_e32 v[228:229], v138
	v_cvt_pk_f32_fp8_sdwa v[230:231], v138 src0_sel:WORD_1
	v_lshlrev_b32_e32 v200, 16, v148
	v_and_b32_e32 v201, 0xffff0000, v148
	v_lshlrev_b32_e32 v202, 16, v149
	v_and_b32_e32 v203, 0xffff0000, v149
	v_pk_fma_f32 v[200:201], v[224:225], v[240:241], v[200:201] op_sel_hi:[1,0,1]
	v_pk_fma_f32 v[202:203], v[226:227], v[240:241], v[202:203] op_sel_hi:[1,0,1]
	v_pk_fma_f32 v[200:201], v[228:229], v[242:243], v[200:201] op_sel_hi:[1,0,1]
	v_pk_fma_f32 v[202:203], v[230:231], v[242:243], v[202:203] op_sel_hi:[1,0,1]
	v_cvt_pk_f32_fp8_e32 v[232:233], v131
	v_cvt_pk_f32_fp8_sdwa v[234:235], v131 src0_sel:WORD_1
	v_cvt_pk_f32_fp8_e32 v[236:237], v139
	v_cvt_pk_f32_fp8_sdwa v[238:239], v139 src0_sel:WORD_1
	v_lshlrev_b32_e32 v204, 16, v150
	v_and_b32_e32 v205, 0xffff0000, v150
	v_lshlrev_b32_e32 v206, 16, v151
	v_and_b32_e32 v207, 0xffff0000, v151
	v_pk_fma_f32 v[204:205], v[232:233], v[240:241], v[204:205] op_sel_hi:[1,0,1]
	v_pk_fma_f32 v[206:207], v[234:235], v[240:241], v[206:207] op_sel_hi:[1,0,1]
	v_pk_fma_f32 v[204:205], v[236:237], v[242:243], v[204:205] op_sel_hi:[1,0,1]
	v_pk_fma_f32 v[206:207], v[238:239], v[242:243], v[206:207] op_sel_hi:[1,0,1]
	v_cvt_pk_f32_fp8_e32 v[224:225], v132
	v_cvt_pk_f32_fp8_sdwa v[226:227], v132 src0_sel:WORD_1
	v_cvt_pk_f32_fp8_e32 v[228:229], v140
	v_cvt_pk_f32_fp8_sdwa v[230:231], v140 src0_sel:WORD_1
	v_lshlrev_b32_e32 v208, 16, v152
	v_and_b32_e32 v209, 0xffff0000, v152
	v_lshlrev_b32_e32 v210, 16, v153
	v_and_b32_e32 v211, 0xffff0000, v153
	v_pk_fma_f32 v[208:209], v[224:225], v[240:241], v[208:209] op_sel_hi:[1,0,1]
	v_pk_fma_f32 v[210:211], v[226:227], v[240:241], v[210:211] op_sel_hi:[1,0,1]
	v_pk_fma_f32 v[208:209], v[228:229], v[242:243], v[208:209] op_sel_hi:[1,0,1]
	v_pk_fma_f32 v[210:211], v[230:231], v[242:243], v[210:211] op_sel_hi:[1,0,1]
	v_cvt_pk_f32_fp8_e32 v[232:233], v133
	v_cvt_pk_f32_fp8_sdwa v[234:235], v133 src0_sel:WORD_1
	v_cvt_pk_f32_fp8_e32 v[236:237], v141
	v_cvt_pk_f32_fp8_sdwa v[238:239], v141 src0_sel:WORD_1
	v_lshlrev_b32_e32 v212, 16, v154
	v_and_b32_e32 v213, 0xffff0000, v154
	v_lshlrev_b32_e32 v214, 16, v155
	v_and_b32_e32 v215, 0xffff0000, v155
	v_pk_fma_f32 v[212:213], v[232:233], v[240:241], v[212:213] op_sel_hi:[1,0,1]
	v_pk_fma_f32 v[214:215], v[234:235], v[240:241], v[214:215] op_sel_hi:[1,0,1]
	v_pk_fma_f32 v[212:213], v[236:237], v[242:243], v[212:213] op_sel_hi:[1,0,1]
	v_pk_fma_f32 v[214:215], v[238:239], v[242:243], v[214:215] op_sel_hi:[1,0,1]
	v_cvt_pk_f32_fp8_e32 v[224:225], v134
	v_cvt_pk_f32_fp8_sdwa v[226:227], v134 src0_sel:WORD_1
	v_cvt_pk_f32_fp8_e32 v[228:229], v142
	v_cvt_pk_f32_fp8_sdwa v[230:231], v142 src0_sel:WORD_1
	v_lshlrev_b32_e32 v216, 16, v156
	v_and_b32_e32 v217, 0xffff0000, v156
	v_lshlrev_b32_e32 v218, 16, v157
	v_and_b32_e32 v219, 0xffff0000, v157
	v_pk_fma_f32 v[216:217], v[224:225], v[240:241], v[216:217] op_sel_hi:[1,0,1]
	v_pk_fma_f32 v[218:219], v[226:227], v[240:241], v[218:219] op_sel_hi:[1,0,1]
	v_pk_fma_f32 v[216:217], v[228:229], v[242:243], v[216:217] op_sel_hi:[1,0,1]
	v_pk_fma_f32 v[218:219], v[230:231], v[242:243], v[218:219] op_sel_hi:[1,0,1]
	v_cvt_pk_f32_fp8_e32 v[232:233], v135
	v_cvt_pk_f32_fp8_sdwa v[234:235], v135 src0_sel:WORD_1
	v_cvt_pk_f32_fp8_e32 v[236:237], v143
	v_cvt_pk_f32_fp8_sdwa v[238:239], v143 src0_sel:WORD_1
	v_lshlrev_b32_e32 v220, 16, v158
	v_and_b32_e32 v221, 0xffff0000, v158
	v_lshlrev_b32_e32 v222, 16, v159
	v_and_b32_e32 v223, 0xffff0000, v159
	v_pk_fma_f32 v[220:221], v[232:233], v[240:241], v[220:221] op_sel_hi:[1,0,1]
	v_pk_fma_f32 v[222:223], v[234:235], v[240:241], v[222:223] op_sel_hi:[1,0,1]
	v_pk_fma_f32 v[220:221], v[236:237], v[242:243], v[220:221] op_sel_hi:[1,0,1]
	v_pk_fma_f32 v[222:223], v[238:239], v[242:243], v[222:223] op_sel_hi:[1,0,1]
	s_waitcnt vmcnt(55)
	s_add_u32 s56, s64, 0x2000000
	s_addc_u32 s57, s65, 0
	s_add_u32 s58, s56, 0x1000
	s_addc_u32 s59, s57, 0
	global_store_dwordx4 v4, v[192:195], s[56:57] nt
	global_store_dwordx4 v4, v[196:199], s[56:57] offset:1024 nt
	global_store_dwordx4 v4, v[200:203], s[56:57] offset:2048 nt
	global_store_dwordx4 v4, v[204:207], s[56:57] offset:3072 nt
	global_store_dwordx4 v4, v[208:211], s[58:59] nt
	global_store_dwordx4 v4, v[212:215], s[58:59] offset:1024 nt
	global_store_dwordx4 v4, v[216:219], s[58:59] offset:2048 nt
	global_store_dwordx4 v4, v[220:223], s[58:59] offset:3072 nt
	s_waitcnt vmcnt(32)
	s_lshl_b32 s50, s21, 11
	s_add_u32 s50, s48, s50
	s_addc_u32 s51, s49, 0
	s_lshl_b32 s52, s29, 11
	s_add_u32 s52, s48, s52
	s_addc_u32 s53, s49, 0
	s_add_u32 s54, s62, 0x2800000
	s_addc_u32 s55, s63, 0
	global_load_dword v128, v2, s[50:51]
	global_load_dword v129, v2, s[50:51] offset:256
	global_load_dword v130, v2, s[50:51] offset:512
	global_load_dword v131, v2, s[50:51] offset:768
	global_load_dword v132, v2, s[50:51] offset:1024
	global_load_dword v133, v2, s[50:51] offset:1280
	global_load_dword v134, v2, s[50:51] offset:1536
	global_load_dword v135, v2, s[50:51] offset:1792
	global_load_dword v136, v2, s[52:53]
	global_load_dword v137, v2, s[52:53] offset:256
	global_load_dword v138, v2, s[52:53] offset:512
	global_load_dword v139, v2, s[52:53] offset:768
	global_load_dword v140, v2, s[52:53] offset:1024
	global_load_dword v141, v2, s[52:53] offset:1280
	global_load_dword v142, v2, s[52:53] offset:1536
	global_load_dword v143, v2, s[52:53] offset:1792
	global_load_dwordx2 v[144:145], v3, s[54:55]
	global_load_dwordx2 v[146:147], v3, s[54:55] offset:512
	global_load_dwordx2 v[148:149], v3, s[54:55] offset:1024
	global_load_dwordx2 v[150:151], v3, s[54:55] offset:1536
	global_load_dwordx2 v[152:153], v3, s[54:55] offset:2048
	global_load_dwordx2 v[154:155], v3, s[54:55] offset:2560
	global_load_dwordx2 v[156:157], v3, s[54:55] offset:3072
	global_load_dwordx2 v[158:159], v3, s[54:55] offset:3584
	v_mov_b32_e32 v240, s35
	v_mov_b32_e32 v242, s43
	v_cvt_pk_f32_fp8_e32 v[224:225], v64
	v_cvt_pk_f32_fp8_sdwa v[226:227], v64 src0_sel:WORD_1
	v_cvt_pk_f32_fp8_e32 v[228:229], v72
	v_cvt_pk_f32_fp8_sdwa v[230:231], v72 src0_sel:WORD_1
	v_lshlrev_b32_e32 v192, 16, v80
	v_and_b32_e32 v193, 0xffff0000, v80
	v_lshlrev_b32_e32 v194, 16, v81
	v_and_b32_e32 v195, 0xffff0000, v81
	v_pk_fma_f32 v[192:193], v[224:225], v[240:241], v[192:193] op_sel_hi:[1,0,1]
	v_pk_fma_f32 v[194:195], v[226:227], v[240:241], v[194:195] op_sel_hi:[1,0,1]
	v_pk_fma_f32 v[192:193], v[228:229], v[242:243], v[192:193] op_sel_hi:[1,0,1]
	v_pk_fma_f32 v[194:195], v[230:231], v[242:243], v[194:195] op_sel_hi:[1,0,1]
	v_cvt_pk_f32_fp8_e32 v[232:233], v65
	v_cvt_pk_f32_fp8_sdwa v[234:235], v65 src0_sel:WORD_1
	v_cvt_pk_f32_fp8_e32 v[236:237], v73
	v_cvt_pk_f32_fp8_sdwa v[238:239], v73 src0_sel:WORD_1
	v_lshlrev_b32_e32 v196, 16, v82
	v_and_b32_e32 v197, 0xffff0000, v82
	v_lshlrev_b32_e32 v198, 16, v83
	v_and_b32_e32 v199, 0xffff0000, v83
	v_pk_fma_f32 v[196:197], v[232:233], v[240:241], v[196:197] op_sel_hi:[1,0,1]
	v_pk_fma_f32 v[198:199], v[234:235], v[240:241], v[198:199] op_sel_hi:[1,0,1]
	v_pk_fma_f32 v[196:197], v[236:237], v[242:243], v[196:197] op_sel_hi:[1,0,1]
	v_pk_fma_f32 v[198:199], v[238:239], v[242:243], v[198:199] op_sel_hi:[1,0,1]
	v_cvt_pk_f32_fp8_e32 v[224:225], v66
	v_cvt_pk_f32_fp8_sdwa v[226:227], v66 src0_sel:WORD_1
	v_cvt_pk_f32_fp8_e32 v[228:229], v74
	v_cvt_pk_f32_fp8_sdwa v[230:231], v74 src0_sel:WORD_1
	v_lshlrev_b32_e32 v200, 16, v84
	v_and_b32_e32 v201, 0xffff0000, v84
	v_lshlrev_b32_e32 v202, 16, v85
	v_and_b32_e32 v203, 0xffff0000, v85
	v_pk_fma_f32 v[200:201], v[224:225], v[240:241], v[200:201] op_sel_hi:[1,0,1]
	v_pk_fma_f32 v[202:203], v[226:227], v[240:241], v[202:203] op_sel_hi:[1,0,1]
	v_pk_fma_f32 v[200:201], v[228:229], v[242:243], v[200:201] op_sel_hi:[1,0,1]
	v_pk_fma_f32 v[202:203], v[230:231], v[242:243], v[202:203] op_sel_hi:[1,0,1]
	v_cvt_pk_f32_fp8_e32 v[232:233], v67
	v_cvt_pk_f32_fp8_sdwa v[234:235], v67 src0_sel:WORD_1
	v_cvt_pk_f32_fp8_e32 v[236:237], v75
	v_cvt_pk_f32_fp8_sdwa v[238:239], v75 src0_sel:WORD_1
	v_lshlrev_b32_e32 v204, 16, v86
	v_and_b32_e32 v205, 0xffff0000, v86
	v_lshlrev_b32_e32 v206, 16, v87
	v_and_b32_e32 v207, 0xffff0000, v87
	v_pk_fma_f32 v[204:205], v[232:233], v[240:241], v[204:205] op_sel_hi:[1,0,1]
	v_pk_fma_f32 v[206:207], v[234:235], v[240:241], v[206:207] op_sel_hi:[1,0,1]
	v_pk_fma_f32 v[204:205], v[236:237], v[242:243], v[204:205] op_sel_hi:[1,0,1]
	v_pk_fma_f32 v[206:207], v[238:239], v[242:243], v[206:207] op_sel_hi:[1,0,1]
	v_cvt_pk_f32_fp8_e32 v[224:225], v68
	v_cvt_pk_f32_fp8_sdwa v[226:227], v68 src0_sel:WORD_1
	v_cvt_pk_f32_fp8_e32 v[228:229], v76
	v_cvt_pk_f32_fp8_sdwa v[230:231], v76 src0_sel:WORD_1
	v_lshlrev_b32_e32 v208, 16, v88
	v_and_b32_e32 v209, 0xffff0000, v88
	v_lshlrev_b32_e32 v210, 16, v89
	v_and_b32_e32 v211, 0xffff0000, v89
	v_pk_fma_f32 v[208:209], v[224:225], v[240:241], v[208:209] op_sel_hi:[1,0,1]
	v_pk_fma_f32 v[210:211], v[226:227], v[240:241], v[210:211] op_sel_hi:[1,0,1]
	v_pk_fma_f32 v[208:209], v[228:229], v[242:243], v[208:209] op_sel_hi:[1,0,1]
	v_pk_fma_f32 v[210:211], v[230:231], v[242:243], v[210:211] op_sel_hi:[1,0,1]
	v_cvt_pk_f32_fp8_e32 v[232:233], v69
	v_cvt_pk_f32_fp8_sdwa v[234:235], v69 src0_sel:WORD_1
	v_cvt_pk_f32_fp8_e32 v[236:237], v77
	v_cvt_pk_f32_fp8_sdwa v[238:239], v77 src0_sel:WORD_1
	v_lshlrev_b32_e32 v212, 16, v90
	v_and_b32_e32 v213, 0xffff0000, v90
	v_lshlrev_b32_e32 v214, 16, v91
	v_and_b32_e32 v215, 0xffff0000, v91
	v_pk_fma_f32 v[212:213], v[232:233], v[240:241], v[212:213] op_sel_hi:[1,0,1]
	v_pk_fma_f32 v[214:215], v[234:235], v[240:241], v[214:215] op_sel_hi:[1,0,1]
	v_pk_fma_f32 v[212:213], v[236:237], v[242:243], v[212:213] op_sel_hi:[1,0,1]
	v_pk_fma_f32 v[214:215], v[238:239], v[242:243], v[214:215] op_sel_hi:[1,0,1]
	v_cvt_pk_f32_fp8_e32 v[224:225], v70
	v_cvt_pk_f32_fp8_sdwa v[226:227], v70 src0_sel:WORD_1
	v_cvt_pk_f32_fp8_e32 v[228:229], v78
	v_cvt_pk_f32_fp8_sdwa v[230:231], v78 src0_sel:WORD_1
	v_lshlrev_b32_e32 v216, 16, v92
	v_and_b32_e32 v217, 0xffff0000, v92
	v_lshlrev_b32_e32 v218, 16, v93
	v_and_b32_e32 v219, 0xffff0000, v93
	v_pk_fma_f32 v[216:217], v[224:225], v[240:241], v[216:217] op_sel_hi:[1,0,1]
	v_pk_fma_f32 v[218:219], v[226:227], v[240:241], v[218:219] op_sel_hi:[1,0,1]
	v_pk_fma_f32 v[216:217], v[228:229], v[242:243], v[216:217] op_sel_hi:[1,0,1]
	v_pk_fma_f32 v[218:219], v[230:231], v[242:243], v[218:219] op_sel_hi:[1,0,1]
	v_cvt_pk_f32_fp8_e32 v[232:233], v71
	v_cvt_pk_f32_fp8_sdwa v[234:235], v71 src0_sel:WORD_1
	v_cvt_pk_f32_fp8_e32 v[236:237], v79
	v_cvt_pk_f32_fp8_sdwa v[238:239], v79 src0_sel:WORD_1
	v_lshlrev_b32_e32 v220, 16, v94
	v_and_b32_e32 v221, 0xffff0000, v94
	v_lshlrev_b32_e32 v222, 16, v95
	v_and_b32_e32 v223, 0xffff0000, v95
	v_pk_fma_f32 v[220:221], v[232:233], v[240:241], v[220:221] op_sel_hi:[1,0,1]
	v_pk_fma_f32 v[222:223], v[234:235], v[240:241], v[222:223] op_sel_hi:[1,0,1]
	v_pk_fma_f32 v[220:221], v[236:237], v[242:243], v[220:221] op_sel_hi:[1,0,1]
	v_pk_fma_f32 v[222:223], v[238:239], v[242:243], v[222:223] op_sel_hi:[1,0,1]
	s_waitcnt vmcnt(55)
	s_add_u32 s56, s64, 0x3000000
	s_addc_u32 s57, s65, 0
	s_add_u32 s58, s56, 0x1000
	s_addc_u32 s59, s57, 0
	global_store_dwordx4 v4, v[192:195], s[56:57] nt
	global_store_dwordx4 v4, v[196:199], s[56:57] offset:1024 nt
	global_store_dwordx4 v4, v[200:203], s[56:57] offset:2048 nt
	global_store_dwordx4 v4, v[204:207], s[56:57] offset:3072 nt
	global_store_dwordx4 v4, v[208:211], s[58:59] nt
	global_store_dwordx4 v4, v[212:215], s[58:59] offset:1024 nt
	global_store_dwordx4 v4, v[216:219], s[58:59] offset:2048 nt
	global_store_dwordx4 v4, v[220:223], s[58:59] offset:3072 nt
	s_waitcnt vmcnt(32)
	s_lshl_b32 s50, s22, 11
	s_add_u32 s50, s48, s50
	s_addc_u32 s51, s49, 0
	s_lshl_b32 s52, s30, 11
	s_add_u32 s52, s48, s52
	s_addc_u32 s53, s49, 0
	s_add_u32 s54, s62, 0x3000000
	s_addc_u32 s55, s63, 0
	global_load_dword v64, v2, s[50:51]
	global_load_dword v65, v2, s[50:51] offset:256
	global_load_dword v66, v2, s[50:51] offset:512
	global_load_dword v67, v2, s[50:51] offset:768
	global_load_dword v68, v2, s[50:51] offset:1024
	global_load_dword v69, v2, s[50:51] offset:1280
	global_load_dword v70, v2, s[50:51] offset:1536
	global_load_dword v71, v2, s[50:51] offset:1792
	global_load_dword v72, v2, s[52:53]
	global_load_dword v73, v2, s[52:53] offset:256
	global_load_dword v74, v2, s[52:53] offset:512
	global_load_dword v75, v2, s[52:53] offset:768
	global_load_dword v76, v2, s[52:53] offset:1024
	global_load_dword v77, v2, s[52:53] offset:1280
	global_load_dword v78, v2, s[52:53] offset:1536
	global_load_dword v79, v2, s[52:53] offset:1792
	global_load_dwordx2 v[80:81], v3, s[54:55]
	global_load_dwordx2 v[82:83], v3, s[54:55] offset:512
	global_load_dwordx2 v[84:85], v3, s[54:55] offset:1024
	global_load_dwordx2 v[86:87], v3, s[54:55] offset:1536
	global_load_dwordx2 v[88:89], v3, s[54:55] offset:2048
	global_load_dwordx2 v[90:91], v3, s[54:55] offset:2560
	global_load_dwordx2 v[92:93], v3, s[54:55] offset:3072
	global_load_dwordx2 v[94:95], v3, s[54:55] offset:3584
	v_mov_b32_e32 v240, s36
	v_mov_b32_e32 v242, s44
	v_cvt_pk_f32_fp8_e32 v[224:225], v96
	v_cvt_pk_f32_fp8_sdwa v[226:227], v96 src0_sel:WORD_1
	v_cvt_pk_f32_fp8_e32 v[228:229], v104
	v_cvt_pk_f32_fp8_sdwa v[230:231], v104 src0_sel:WORD_1
	v_lshlrev_b32_e32 v192, 16, v112
	v_and_b32_e32 v193, 0xffff0000, v112
	v_lshlrev_b32_e32 v194, 16, v113
	v_and_b32_e32 v195, 0xffff0000, v113
	v_pk_fma_f32 v[192:193], v[224:225], v[240:241], v[192:193] op_sel_hi:[1,0,1]
	v_pk_fma_f32 v[194:195], v[226:227], v[240:241], v[194:195] op_sel_hi:[1,0,1]
	v_pk_fma_f32 v[192:193], v[228:229], v[242:243], v[192:193] op_sel_hi:[1,0,1]
	v_pk_fma_f32 v[194:195], v[230:231], v[242:243], v[194:195] op_sel_hi:[1,0,1]
	v_cvt_pk_f32_fp8_e32 v[232:233], v97
	v_cvt_pk_f32_fp8_sdwa v[234:235], v97 src0_sel:WORD_1
	v_cvt_pk_f32_fp8_e32 v[236:237], v105
	v_cvt_pk_f32_fp8_sdwa v[238:239], v105 src0_sel:WORD_1
	v_lshlrev_b32_e32 v196, 16, v114
	v_and_b32_e32 v197, 0xffff0000, v114
	v_lshlrev_b32_e32 v198, 16, v115
	v_and_b32_e32 v199, 0xffff0000, v115
	v_pk_fma_f32 v[196:197], v[232:233], v[240:241], v[196:197] op_sel_hi:[1,0,1]
	v_pk_fma_f32 v[198:199], v[234:235], v[240:241], v[198:199] op_sel_hi:[1,0,1]
	v_pk_fma_f32 v[196:197], v[236:237], v[242:243], v[196:197] op_sel_hi:[1,0,1]
	v_pk_fma_f32 v[198:199], v[238:239], v[242:243], v[198:199] op_sel_hi:[1,0,1]
	v_cvt_pk_f32_fp8_e32 v[224:225], v98
	v_cvt_pk_f32_fp8_sdwa v[226:227], v98 src0_sel:WORD_1
	v_cvt_pk_f32_fp8_e32 v[228:229], v106
	v_cvt_pk_f32_fp8_sdwa v[230:231], v106 src0_sel:WORD_1
	v_lshlrev_b32_e32 v200, 16, v116
	v_and_b32_e32 v201, 0xffff0000, v116
	v_lshlrev_b32_e32 v202, 16, v117
	v_and_b32_e32 v203, 0xffff0000, v117
	v_pk_fma_f32 v[200:201], v[224:225], v[240:241], v[200:201] op_sel_hi:[1,0,1]
	v_pk_fma_f32 v[202:203], v[226:227], v[240:241], v[202:203] op_sel_hi:[1,0,1]
	v_pk_fma_f32 v[200:201], v[228:229], v[242:243], v[200:201] op_sel_hi:[1,0,1]
	v_pk_fma_f32 v[202:203], v[230:231], v[242:243], v[202:203] op_sel_hi:[1,0,1]
	v_cvt_pk_f32_fp8_e32 v[232:233], v99
	v_cvt_pk_f32_fp8_sdwa v[234:235], v99 src0_sel:WORD_1
	v_cvt_pk_f32_fp8_e32 v[236:237], v107
	v_cvt_pk_f32_fp8_sdwa v[238:239], v107 src0_sel:WORD_1
	v_lshlrev_b32_e32 v204, 16, v118
	v_and_b32_e32 v205, 0xffff0000, v118
	v_lshlrev_b32_e32 v206, 16, v119
	v_and_b32_e32 v207, 0xffff0000, v119
	v_pk_fma_f32 v[204:205], v[232:233], v[240:241], v[204:205] op_sel_hi:[1,0,1]
	v_pk_fma_f32 v[206:207], v[234:235], v[240:241], v[206:207] op_sel_hi:[1,0,1]
	v_pk_fma_f32 v[204:205], v[236:237], v[242:243], v[204:205] op_sel_hi:[1,0,1]
	v_pk_fma_f32 v[206:207], v[238:239], v[242:243], v[206:207] op_sel_hi:[1,0,1]
	v_cvt_pk_f32_fp8_e32 v[224:225], v100
	v_cvt_pk_f32_fp8_sdwa v[226:227], v100 src0_sel:WORD_1
	v_cvt_pk_f32_fp8_e32 v[228:229], v108
	v_cvt_pk_f32_fp8_sdwa v[230:231], v108 src0_sel:WORD_1
	v_lshlrev_b32_e32 v208, 16, v120
	v_and_b32_e32 v209, 0xffff0000, v120
	v_lshlrev_b32_e32 v210, 16, v121
	v_and_b32_e32 v211, 0xffff0000, v121
	v_pk_fma_f32 v[208:209], v[224:225], v[240:241], v[208:209] op_sel_hi:[1,0,1]
	v_pk_fma_f32 v[210:211], v[226:227], v[240:241], v[210:211] op_sel_hi:[1,0,1]
	v_pk_fma_f32 v[208:209], v[228:229], v[242:243], v[208:209] op_sel_hi:[1,0,1]
	v_pk_fma_f32 v[210:211], v[230:231], v[242:243], v[210:211] op_sel_hi:[1,0,1]
	v_cvt_pk_f32_fp8_e32 v[232:233], v101
	v_cvt_pk_f32_fp8_sdwa v[234:235], v101 src0_sel:WORD_1
	v_cvt_pk_f32_fp8_e32 v[236:237], v109
	v_cvt_pk_f32_fp8_sdwa v[238:239], v109 src0_sel:WORD_1
	v_lshlrev_b32_e32 v212, 16, v122
	v_and_b32_e32 v213, 0xffff0000, v122
	v_lshlrev_b32_e32 v214, 16, v123
	v_and_b32_e32 v215, 0xffff0000, v123
	v_pk_fma_f32 v[212:213], v[232:233], v[240:241], v[212:213] op_sel_hi:[1,0,1]
	v_pk_fma_f32 v[214:215], v[234:235], v[240:241], v[214:215] op_sel_hi:[1,0,1]
	v_pk_fma_f32 v[212:213], v[236:237], v[242:243], v[212:213] op_sel_hi:[1,0,1]
	v_pk_fma_f32 v[214:215], v[238:239], v[242:243], v[214:215] op_sel_hi:[1,0,1]
	v_cvt_pk_f32_fp8_e32 v[224:225], v102
	v_cvt_pk_f32_fp8_sdwa v[226:227], v102 src0_sel:WORD_1
	v_cvt_pk_f32_fp8_e32 v[228:229], v110
	v_cvt_pk_f32_fp8_sdwa v[230:231], v110 src0_sel:WORD_1
	v_lshlrev_b32_e32 v216, 16, v124
	v_and_b32_e32 v217, 0xffff0000, v124
	v_lshlrev_b32_e32 v218, 16, v125
	v_and_b32_e32 v219, 0xffff0000, v125
	v_pk_fma_f32 v[216:217], v[224:225], v[240:241], v[216:217] op_sel_hi:[1,0,1]
	v_pk_fma_f32 v[218:219], v[226:227], v[240:241], v[218:219] op_sel_hi:[1,0,1]
	v_pk_fma_f32 v[216:217], v[228:229], v[242:243], v[216:217] op_sel_hi:[1,0,1]
	v_pk_fma_f32 v[218:219], v[230:231], v[242:243], v[218:219] op_sel_hi:[1,0,1]
	v_cvt_pk_f32_fp8_e32 v[232:233], v103
	v_cvt_pk_f32_fp8_sdwa v[234:235], v103 src0_sel:WORD_1
	v_cvt_pk_f32_fp8_e32 v[236:237], v111
	v_cvt_pk_f32_fp8_sdwa v[238:239], v111 src0_sel:WORD_1
	v_lshlrev_b32_e32 v220, 16, v126
	v_and_b32_e32 v221, 0xffff0000, v126
	v_lshlrev_b32_e32 v222, 16, v127
	v_and_b32_e32 v223, 0xffff0000, v127
	v_pk_fma_f32 v[220:221], v[232:233], v[240:241], v[220:221] op_sel_hi:[1,0,1]
	v_pk_fma_f32 v[222:223], v[234:235], v[240:241], v[222:223] op_sel_hi:[1,0,1]
	v_pk_fma_f32 v[220:221], v[236:237], v[242:243], v[220:221] op_sel_hi:[1,0,1]
	v_pk_fma_f32 v[222:223], v[238:239], v[242:243], v[222:223] op_sel_hi:[1,0,1]
	s_waitcnt vmcnt(55)
	s_add_u32 s56, s64, 0x4000000
	s_addc_u32 s57, s65, 0
	s_add_u32 s58, s56, 0x1000
	s_addc_u32 s59, s57, 0
	global_store_dwordx4 v4, v[192:195], s[56:57] nt
	global_store_dwordx4 v4, v[196:199], s[56:57] offset:1024 nt
	global_store_dwordx4 v4, v[200:203], s[56:57] offset:2048 nt
	global_store_dwordx4 v4, v[204:207], s[56:57] offset:3072 nt
	global_store_dwordx4 v4, v[208:211], s[58:59] nt
	global_store_dwordx4 v4, v[212:215], s[58:59] offset:1024 nt
	global_store_dwordx4 v4, v[216:219], s[58:59] offset:2048 nt
	global_store_dwordx4 v4, v[220:223], s[58:59] offset:3072 nt
	s_waitcnt vmcnt(32)
	s_lshl_b32 s50, s23, 11
	s_add_u32 s50, s48, s50
	s_addc_u32 s51, s49, 0
	s_lshl_b32 s52, s31, 11
	s_add_u32 s52, s48, s52
	s_addc_u32 s53, s49, 0
	s_add_u32 s54, s62, 0x3800000
	s_addc_u32 s55, s63, 0
	global_load_dword v96, v2, s[50:51]
	global_load_dword v97, v2, s[50:51] offset:256
	global_load_dword v98, v2, s[50:51] offset:512
	global_load_dword v99, v2, s[50:51] offset:768
	global_load_dword v100, v2, s[50:51] offset:1024
	global_load_dword v101, v2, s[50:51] offset:1280
	global_load_dword v102, v2, s[50:51] offset:1536
	global_load_dword v103, v2, s[50:51] offset:1792
	global_load_dword v104, v2, s[52:53]
	global_load_dword v105, v2, s[52:53] offset:256
	global_load_dword v106, v2, s[52:53] offset:512
	global_load_dword v107, v2, s[52:53] offset:768
	global_load_dword v108, v2, s[52:53] offset:1024
	global_load_dword v109, v2, s[52:53] offset:1280
	global_load_dword v110, v2, s[52:53] offset:1536
	global_load_dword v111, v2, s[52:53] offset:1792
	global_load_dwordx2 v[112:113], v3, s[54:55]
	global_load_dwordx2 v[114:115], v3, s[54:55] offset:512
	global_load_dwordx2 v[116:117], v3, s[54:55] offset:1024
	global_load_dwordx2 v[118:119], v3, s[54:55] offset:1536
	global_load_dwordx2 v[120:121], v3, s[54:55] offset:2048
	global_load_dwordx2 v[122:123], v3, s[54:55] offset:2560
	global_load_dwordx2 v[124:125], v3, s[54:55] offset:3072
	global_load_dwordx2 v[126:127], v3, s[54:55] offset:3584
	v_mov_b32_e32 v240, s37
	v_mov_b32_e32 v242, s45
	v_cvt_pk_f32_fp8_e32 v[224:225], v128
	v_cvt_pk_f32_fp8_sdwa v[226:227], v128 src0_sel:WORD_1
	v_cvt_pk_f32_fp8_e32 v[228:229], v136
	v_cvt_pk_f32_fp8_sdwa v[230:231], v136 src0_sel:WORD_1
	v_lshlrev_b32_e32 v192, 16, v144
	v_and_b32_e32 v193, 0xffff0000, v144
	v_lshlrev_b32_e32 v194, 16, v145
	v_and_b32_e32 v195, 0xffff0000, v145
	v_pk_fma_f32 v[192:193], v[224:225], v[240:241], v[192:193] op_sel_hi:[1,0,1]
	v_pk_fma_f32 v[194:195], v[226:227], v[240:241], v[194:195] op_sel_hi:[1,0,1]
	v_pk_fma_f32 v[192:193], v[228:229], v[242:243], v[192:193] op_sel_hi:[1,0,1]
	v_pk_fma_f32 v[194:195], v[230:231], v[242:243], v[194:195] op_sel_hi:[1,0,1]
	v_cvt_pk_f32_fp8_e32 v[232:233], v129
	v_cvt_pk_f32_fp8_sdwa v[234:235], v129 src0_sel:WORD_1
	v_cvt_pk_f32_fp8_e32 v[236:237], v137
	v_cvt_pk_f32_fp8_sdwa v[238:239], v137 src0_sel:WORD_1
	v_lshlrev_b32_e32 v196, 16, v146
	v_and_b32_e32 v197, 0xffff0000, v146
	v_lshlrev_b32_e32 v198, 16, v147
	v_and_b32_e32 v199, 0xffff0000, v147
	v_pk_fma_f32 v[196:197], v[232:233], v[240:241], v[196:197] op_sel_hi:[1,0,1]
	v_pk_fma_f32 v[198:199], v[234:235], v[240:241], v[198:199] op_sel_hi:[1,0,1]
	v_pk_fma_f32 v[196:197], v[236:237], v[242:243], v[196:197] op_sel_hi:[1,0,1]
	v_pk_fma_f32 v[198:199], v[238:239], v[242:243], v[198:199] op_sel_hi:[1,0,1]
	v_cvt_pk_f32_fp8_e32 v[224:225], v130
	v_cvt_pk_f32_fp8_sdwa v[226:227], v130 src0_sel:WORD_1
	v_cvt_pk_f32_fp8_e32 v[228:229], v138
	v_cvt_pk_f32_fp8_sdwa v[230:231], v138 src0_sel:WORD_1
	v_lshlrev_b32_e32 v200, 16, v148
	v_and_b32_e32 v201, 0xffff0000, v148
	v_lshlrev_b32_e32 v202, 16, v149
	v_and_b32_e32 v203, 0xffff0000, v149
	v_pk_fma_f32 v[200:201], v[224:225], v[240:241], v[200:201] op_sel_hi:[1,0,1]
	v_pk_fma_f32 v[202:203], v[226:227], v[240:241], v[202:203] op_sel_hi:[1,0,1]
	v_pk_fma_f32 v[200:201], v[228:229], v[242:243], v[200:201] op_sel_hi:[1,0,1]
	v_pk_fma_f32 v[202:203], v[230:231], v[242:243], v[202:203] op_sel_hi:[1,0,1]
	v_cvt_pk_f32_fp8_e32 v[232:233], v131
	v_cvt_pk_f32_fp8_sdwa v[234:235], v131 src0_sel:WORD_1
	v_cvt_pk_f32_fp8_e32 v[236:237], v139
	v_cvt_pk_f32_fp8_sdwa v[238:239], v139 src0_sel:WORD_1
	v_lshlrev_b32_e32 v204, 16, v150
	v_and_b32_e32 v205, 0xffff0000, v150
	v_lshlrev_b32_e32 v206, 16, v151
	v_and_b32_e32 v207, 0xffff0000, v151
	v_pk_fma_f32 v[204:205], v[232:233], v[240:241], v[204:205] op_sel_hi:[1,0,1]
	v_pk_fma_f32 v[206:207], v[234:235], v[240:241], v[206:207] op_sel_hi:[1,0,1]
	v_pk_fma_f32 v[204:205], v[236:237], v[242:243], v[204:205] op_sel_hi:[1,0,1]
	v_pk_fma_f32 v[206:207], v[238:239], v[242:243], v[206:207] op_sel_hi:[1,0,1]
	v_cvt_pk_f32_fp8_e32 v[224:225], v132
	v_cvt_pk_f32_fp8_sdwa v[226:227], v132 src0_sel:WORD_1
	v_cvt_pk_f32_fp8_e32 v[228:229], v140
	v_cvt_pk_f32_fp8_sdwa v[230:231], v140 src0_sel:WORD_1
	v_lshlrev_b32_e32 v208, 16, v152
	v_and_b32_e32 v209, 0xffff0000, v152
	v_lshlrev_b32_e32 v210, 16, v153
	v_and_b32_e32 v211, 0xffff0000, v153
	v_pk_fma_f32 v[208:209], v[224:225], v[240:241], v[208:209] op_sel_hi:[1,0,1]
	v_pk_fma_f32 v[210:211], v[226:227], v[240:241], v[210:211] op_sel_hi:[1,0,1]
	v_pk_fma_f32 v[208:209], v[228:229], v[242:243], v[208:209] op_sel_hi:[1,0,1]
	v_pk_fma_f32 v[210:211], v[230:231], v[242:243], v[210:211] op_sel_hi:[1,0,1]
	v_cvt_pk_f32_fp8_e32 v[232:233], v133
	v_cvt_pk_f32_fp8_sdwa v[234:235], v133 src0_sel:WORD_1
	v_cvt_pk_f32_fp8_e32 v[236:237], v141
	v_cvt_pk_f32_fp8_sdwa v[238:239], v141 src0_sel:WORD_1
	v_lshlrev_b32_e32 v212, 16, v154
	v_and_b32_e32 v213, 0xffff0000, v154
	v_lshlrev_b32_e32 v214, 16, v155
	v_and_b32_e32 v215, 0xffff0000, v155
	v_pk_fma_f32 v[212:213], v[232:233], v[240:241], v[212:213] op_sel_hi:[1,0,1]
	v_pk_fma_f32 v[214:215], v[234:235], v[240:241], v[214:215] op_sel_hi:[1,0,1]
	v_pk_fma_f32 v[212:213], v[236:237], v[242:243], v[212:213] op_sel_hi:[1,0,1]
	v_pk_fma_f32 v[214:215], v[238:239], v[242:243], v[214:215] op_sel_hi:[1,0,1]
	v_cvt_pk_f32_fp8_e32 v[224:225], v134
	v_cvt_pk_f32_fp8_sdwa v[226:227], v134 src0_sel:WORD_1
	v_cvt_pk_f32_fp8_e32 v[228:229], v142
	v_cvt_pk_f32_fp8_sdwa v[230:231], v142 src0_sel:WORD_1
	v_lshlrev_b32_e32 v216, 16, v156
	v_and_b32_e32 v217, 0xffff0000, v156
	v_lshlrev_b32_e32 v218, 16, v157
	v_and_b32_e32 v219, 0xffff0000, v157
	v_pk_fma_f32 v[216:217], v[224:225], v[240:241], v[216:217] op_sel_hi:[1,0,1]
	v_pk_fma_f32 v[218:219], v[226:227], v[240:241], v[218:219] op_sel_hi:[1,0,1]
	v_pk_fma_f32 v[216:217], v[228:229], v[242:243], v[216:217] op_sel_hi:[1,0,1]
	v_pk_fma_f32 v[218:219], v[230:231], v[242:243], v[218:219] op_sel_hi:[1,0,1]
	v_cvt_pk_f32_fp8_e32 v[232:233], v135
	v_cvt_pk_f32_fp8_sdwa v[234:235], v135 src0_sel:WORD_1
	v_cvt_pk_f32_fp8_e32 v[236:237], v143
	v_cvt_pk_f32_fp8_sdwa v[238:239], v143 src0_sel:WORD_1
	v_lshlrev_b32_e32 v220, 16, v158
	v_and_b32_e32 v221, 0xffff0000, v158
	v_lshlrev_b32_e32 v222, 16, v159
	v_and_b32_e32 v223, 0xffff0000, v159
	v_pk_fma_f32 v[220:221], v[232:233], v[240:241], v[220:221] op_sel_hi:[1,0,1]
	v_pk_fma_f32 v[222:223], v[234:235], v[240:241], v[222:223] op_sel_hi:[1,0,1]
	v_pk_fma_f32 v[220:221], v[236:237], v[242:243], v[220:221] op_sel_hi:[1,0,1]
	v_pk_fma_f32 v[222:223], v[238:239], v[242:243], v[222:223] op_sel_hi:[1,0,1]
	s_waitcnt vmcnt(55)
	s_add_u32 s56, s64, 0x5000000
	s_addc_u32 s57, s65, 0
	s_add_u32 s58, s56, 0x1000
	s_addc_u32 s59, s57, 0
	global_store_dwordx4 v4, v[192:195], s[56:57] nt
	global_store_dwordx4 v4, v[196:199], s[56:57] offset:1024 nt
	global_store_dwordx4 v4, v[200:203], s[56:57] offset:2048 nt
	global_store_dwordx4 v4, v[204:207], s[56:57] offset:3072 nt
	global_store_dwordx4 v4, v[208:211], s[58:59] nt
	global_store_dwordx4 v4, v[212:215], s[58:59] offset:1024 nt
	global_store_dwordx4 v4, v[216:219], s[58:59] offset:2048 nt
	global_store_dwordx4 v4, v[220:223], s[58:59] offset:3072 nt
	s_waitcnt vmcnt(32)
	v_mov_b32_e32 v240, s38
	v_mov_b32_e32 v242, s46
	v_cvt_pk_f32_fp8_e32 v[224:225], v64
	v_cvt_pk_f32_fp8_sdwa v[226:227], v64 src0_sel:WORD_1
	v_cvt_pk_f32_fp8_e32 v[228:229], v72
	v_cvt_pk_f32_fp8_sdwa v[230:231], v72 src0_sel:WORD_1
	v_lshlrev_b32_e32 v192, 16, v80
	v_and_b32_e32 v193, 0xffff0000, v80
	v_lshlrev_b32_e32 v194, 16, v81
	v_and_b32_e32 v195, 0xffff0000, v81
	v_pk_fma_f32 v[192:193], v[224:225], v[240:241], v[192:193] op_sel_hi:[1,0,1]
	v_pk_fma_f32 v[194:195], v[226:227], v[240:241], v[194:195] op_sel_hi:[1,0,1]
	v_pk_fma_f32 v[192:193], v[228:229], v[242:243], v[192:193] op_sel_hi:[1,0,1]
	v_pk_fma_f32 v[194:195], v[230:231], v[242:243], v[194:195] op_sel_hi:[1,0,1]
	v_cvt_pk_f32_fp8_e32 v[232:233], v65
	v_cvt_pk_f32_fp8_sdwa v[234:235], v65 src0_sel:WORD_1
	v_cvt_pk_f32_fp8_e32 v[236:237], v73
	v_cvt_pk_f32_fp8_sdwa v[238:239], v73 src0_sel:WORD_1
	v_lshlrev_b32_e32 v196, 16, v82
	v_and_b32_e32 v197, 0xffff0000, v82
	v_lshlrev_b32_e32 v198, 16, v83
	v_and_b32_e32 v199, 0xffff0000, v83
	v_pk_fma_f32 v[196:197], v[232:233], v[240:241], v[196:197] op_sel_hi:[1,0,1]
	v_pk_fma_f32 v[198:199], v[234:235], v[240:241], v[198:199] op_sel_hi:[1,0,1]
	v_pk_fma_f32 v[196:197], v[236:237], v[242:243], v[196:197] op_sel_hi:[1,0,1]
	v_pk_fma_f32 v[198:199], v[238:239], v[242:243], v[198:199] op_sel_hi:[1,0,1]
	v_cvt_pk_f32_fp8_e32 v[224:225], v66
	v_cvt_pk_f32_fp8_sdwa v[226:227], v66 src0_sel:WORD_1
	v_cvt_pk_f32_fp8_e32 v[228:229], v74
	v_cvt_pk_f32_fp8_sdwa v[230:231], v74 src0_sel:WORD_1
	v_lshlrev_b32_e32 v200, 16, v84
	v_and_b32_e32 v201, 0xffff0000, v84
	v_lshlrev_b32_e32 v202, 16, v85
	v_and_b32_e32 v203, 0xffff0000, v85
	v_pk_fma_f32 v[200:201], v[224:225], v[240:241], v[200:201] op_sel_hi:[1,0,1]
	v_pk_fma_f32 v[202:203], v[226:227], v[240:241], v[202:203] op_sel_hi:[1,0,1]
	v_pk_fma_f32 v[200:201], v[228:229], v[242:243], v[200:201] op_sel_hi:[1,0,1]
	v_pk_fma_f32 v[202:203], v[230:231], v[242:243], v[202:203] op_sel_hi:[1,0,1]
	v_cvt_pk_f32_fp8_e32 v[232:233], v67
	v_cvt_pk_f32_fp8_sdwa v[234:235], v67 src0_sel:WORD_1
	v_cvt_pk_f32_fp8_e32 v[236:237], v75
	v_cvt_pk_f32_fp8_sdwa v[238:239], v75 src0_sel:WORD_1
	v_lshlrev_b32_e32 v204, 16, v86
	v_and_b32_e32 v205, 0xffff0000, v86
	v_lshlrev_b32_e32 v206, 16, v87
	v_and_b32_e32 v207, 0xffff0000, v87
	v_pk_fma_f32 v[204:205], v[232:233], v[240:241], v[204:205] op_sel_hi:[1,0,1]
	v_pk_fma_f32 v[206:207], v[234:235], v[240:241], v[206:207] op_sel_hi:[1,0,1]
	v_pk_fma_f32 v[204:205], v[236:237], v[242:243], v[204:205] op_sel_hi:[1,0,1]
	v_pk_fma_f32 v[206:207], v[238:239], v[242:243], v[206:207] op_sel_hi:[1,0,1]
	v_cvt_pk_f32_fp8_e32 v[224:225], v68
	v_cvt_pk_f32_fp8_sdwa v[226:227], v68 src0_sel:WORD_1
	v_cvt_pk_f32_fp8_e32 v[228:229], v76
	v_cvt_pk_f32_fp8_sdwa v[230:231], v76 src0_sel:WORD_1
	v_lshlrev_b32_e32 v208, 16, v88
	v_and_b32_e32 v209, 0xffff0000, v88
	v_lshlrev_b32_e32 v210, 16, v89
	v_and_b32_e32 v211, 0xffff0000, v89
	v_pk_fma_f32 v[208:209], v[224:225], v[240:241], v[208:209] op_sel_hi:[1,0,1]
	v_pk_fma_f32 v[210:211], v[226:227], v[240:241], v[210:211] op_sel_hi:[1,0,1]
	v_pk_fma_f32 v[208:209], v[228:229], v[242:243], v[208:209] op_sel_hi:[1,0,1]
	v_pk_fma_f32 v[210:211], v[230:231], v[242:243], v[210:211] op_sel_hi:[1,0,1]
	v_cvt_pk_f32_fp8_e32 v[232:233], v69
	v_cvt_pk_f32_fp8_sdwa v[234:235], v69 src0_sel:WORD_1
	v_cvt_pk_f32_fp8_e32 v[236:237], v77
	v_cvt_pk_f32_fp8_sdwa v[238:239], v77 src0_sel:WORD_1
	v_lshlrev_b32_e32 v212, 16, v90
	v_and_b32_e32 v213, 0xffff0000, v90
	v_lshlrev_b32_e32 v214, 16, v91
	v_and_b32_e32 v215, 0xffff0000, v91
	v_pk_fma_f32 v[212:213], v[232:233], v[240:241], v[212:213] op_sel_hi:[1,0,1]
	v_pk_fma_f32 v[214:215], v[234:235], v[240:241], v[214:215] op_sel_hi:[1,0,1]
	v_pk_fma_f32 v[212:213], v[236:237], v[242:243], v[212:213] op_sel_hi:[1,0,1]
	v_pk_fma_f32 v[214:215], v[238:239], v[242:243], v[214:215] op_sel_hi:[1,0,1]
	v_cvt_pk_f32_fp8_e32 v[224:225], v70
	v_cvt_pk_f32_fp8_sdwa v[226:227], v70 src0_sel:WORD_1
	v_cvt_pk_f32_fp8_e32 v[228:229], v78
	v_cvt_pk_f32_fp8_sdwa v[230:231], v78 src0_sel:WORD_1
	v_lshlrev_b32_e32 v216, 16, v92
	v_and_b32_e32 v217, 0xffff0000, v92
	v_lshlrev_b32_e32 v218, 16, v93
	v_and_b32_e32 v219, 0xffff0000, v93
	v_pk_fma_f32 v[216:217], v[224:225], v[240:241], v[216:217] op_sel_hi:[1,0,1]
	v_pk_fma_f32 v[218:219], v[226:227], v[240:241], v[218:219] op_sel_hi:[1,0,1]
	v_pk_fma_f32 v[216:217], v[228:229], v[242:243], v[216:217] op_sel_hi:[1,0,1]
	v_pk_fma_f32 v[218:219], v[230:231], v[242:243], v[218:219] op_sel_hi:[1,0,1]
	v_cvt_pk_f32_fp8_e32 v[232:233], v71
	v_cvt_pk_f32_fp8_sdwa v[234:235], v71 src0_sel:WORD_1
	v_cvt_pk_f32_fp8_e32 v[236:237], v79
	v_cvt_pk_f32_fp8_sdwa v[238:239], v79 src0_sel:WORD_1
	v_lshlrev_b32_e32 v220, 16, v94
	v_and_b32_e32 v221, 0xffff0000, v94
	v_lshlrev_b32_e32 v222, 16, v95
	v_and_b32_e32 v223, 0xffff0000, v95
	v_pk_fma_f32 v[220:221], v[232:233], v[240:241], v[220:221] op_sel_hi:[1,0,1]
	v_pk_fma_f32 v[222:223], v[234:235], v[240:241], v[222:223] op_sel_hi:[1,0,1]
	v_pk_fma_f32 v[220:221], v[236:237], v[242:243], v[220:221] op_sel_hi:[1,0,1]
	v_pk_fma_f32 v[222:223], v[238:239], v[242:243], v[222:223] op_sel_hi:[1,0,1]
	s_waitcnt vmcnt(55)
	s_add_u32 s56, s64, 0x6000000
	s_addc_u32 s57, s65, 0
	s_add_u32 s58, s56, 0x1000
	s_addc_u32 s59, s57, 0
	global_store_dwordx4 v4, v[192:195], s[56:57] nt
	global_store_dwordx4 v4, v[196:199], s[56:57] offset:1024 nt
	global_store_dwordx4 v4, v[200:203], s[56:57] offset:2048 nt
	global_store_dwordx4 v4, v[204:207], s[56:57] offset:3072 nt
	global_store_dwordx4 v4, v[208:211], s[58:59] nt
	global_store_dwordx4 v4, v[212:215], s[58:59] offset:1024 nt
	global_store_dwordx4 v4, v[216:219], s[58:59] offset:2048 nt
	global_store_dwordx4 v4, v[220:223], s[58:59] offset:3072 nt
	s_waitcnt vmcnt(16)
	v_mov_b32_e32 v240, s39
	v_mov_b32_e32 v242, s47
	v_cvt_pk_f32_fp8_e32 v[224:225], v96
	v_cvt_pk_f32_fp8_sdwa v[226:227], v96 src0_sel:WORD_1
	v_cvt_pk_f32_fp8_e32 v[228:229], v104
	v_cvt_pk_f32_fp8_sdwa v[230:231], v104 src0_sel:WORD_1
	v_lshlrev_b32_e32 v192, 16, v112
	v_and_b32_e32 v193, 0xffff0000, v112
	v_lshlrev_b32_e32 v194, 16, v113
	v_and_b32_e32 v195, 0xffff0000, v113
	v_pk_fma_f32 v[192:193], v[224:225], v[240:241], v[192:193] op_sel_hi:[1,0,1]
	v_pk_fma_f32 v[194:195], v[226:227], v[240:241], v[194:195] op_sel_hi:[1,0,1]
	v_pk_fma_f32 v[192:193], v[228:229], v[242:243], v[192:193] op_sel_hi:[1,0,1]
	v_pk_fma_f32 v[194:195], v[230:231], v[242:243], v[194:195] op_sel_hi:[1,0,1]
	v_cvt_pk_f32_fp8_e32 v[232:233], v97
	v_cvt_pk_f32_fp8_sdwa v[234:235], v97 src0_sel:WORD_1
	v_cvt_pk_f32_fp8_e32 v[236:237], v105
	v_cvt_pk_f32_fp8_sdwa v[238:239], v105 src0_sel:WORD_1
	v_lshlrev_b32_e32 v196, 16, v114
	v_and_b32_e32 v197, 0xffff0000, v114
	v_lshlrev_b32_e32 v198, 16, v115
	v_and_b32_e32 v199, 0xffff0000, v115
	v_pk_fma_f32 v[196:197], v[232:233], v[240:241], v[196:197] op_sel_hi:[1,0,1]
	v_pk_fma_f32 v[198:199], v[234:235], v[240:241], v[198:199] op_sel_hi:[1,0,1]
	v_pk_fma_f32 v[196:197], v[236:237], v[242:243], v[196:197] op_sel_hi:[1,0,1]
	v_pk_fma_f32 v[198:199], v[238:239], v[242:243], v[198:199] op_sel_hi:[1,0,1]
	v_cvt_pk_f32_fp8_e32 v[224:225], v98
	v_cvt_pk_f32_fp8_sdwa v[226:227], v98 src0_sel:WORD_1
	v_cvt_pk_f32_fp8_e32 v[228:229], v106
	v_cvt_pk_f32_fp8_sdwa v[230:231], v106 src0_sel:WORD_1
	v_lshlrev_b32_e32 v200, 16, v116
	v_and_b32_e32 v201, 0xffff0000, v116
	v_lshlrev_b32_e32 v202, 16, v117
	v_and_b32_e32 v203, 0xffff0000, v117
	v_pk_fma_f32 v[200:201], v[224:225], v[240:241], v[200:201] op_sel_hi:[1,0,1]
	v_pk_fma_f32 v[202:203], v[226:227], v[240:241], v[202:203] op_sel_hi:[1,0,1]
	v_pk_fma_f32 v[200:201], v[228:229], v[242:243], v[200:201] op_sel_hi:[1,0,1]
	v_pk_fma_f32 v[202:203], v[230:231], v[242:243], v[202:203] op_sel_hi:[1,0,1]
	v_cvt_pk_f32_fp8_e32 v[232:233], v99
	v_cvt_pk_f32_fp8_sdwa v[234:235], v99 src0_sel:WORD_1
	v_cvt_pk_f32_fp8_e32 v[236:237], v107
	v_cvt_pk_f32_fp8_sdwa v[238:239], v107 src0_sel:WORD_1
	v_lshlrev_b32_e32 v204, 16, v118
	v_and_b32_e32 v205, 0xffff0000, v118
	v_lshlrev_b32_e32 v206, 16, v119
	v_and_b32_e32 v207, 0xffff0000, v119
	v_pk_fma_f32 v[204:205], v[232:233], v[240:241], v[204:205] op_sel_hi:[1,0,1]
	v_pk_fma_f32 v[206:207], v[234:235], v[240:241], v[206:207] op_sel_hi:[1,0,1]
	v_pk_fma_f32 v[204:205], v[236:237], v[242:243], v[204:205] op_sel_hi:[1,0,1]
	v_pk_fma_f32 v[206:207], v[238:239], v[242:243], v[206:207] op_sel_hi:[1,0,1]
	v_cvt_pk_f32_fp8_e32 v[224:225], v100
	v_cvt_pk_f32_fp8_sdwa v[226:227], v100 src0_sel:WORD_1
	v_cvt_pk_f32_fp8_e32 v[228:229], v108
	v_cvt_pk_f32_fp8_sdwa v[230:231], v108 src0_sel:WORD_1
	v_lshlrev_b32_e32 v208, 16, v120
	v_and_b32_e32 v209, 0xffff0000, v120
	v_lshlrev_b32_e32 v210, 16, v121
	v_and_b32_e32 v211, 0xffff0000, v121
	v_pk_fma_f32 v[208:209], v[224:225], v[240:241], v[208:209] op_sel_hi:[1,0,1]
	v_pk_fma_f32 v[210:211], v[226:227], v[240:241], v[210:211] op_sel_hi:[1,0,1]
	v_pk_fma_f32 v[208:209], v[228:229], v[242:243], v[208:209] op_sel_hi:[1,0,1]
	v_pk_fma_f32 v[210:211], v[230:231], v[242:243], v[210:211] op_sel_hi:[1,0,1]
	v_cvt_pk_f32_fp8_e32 v[232:233], v101
	v_cvt_pk_f32_fp8_sdwa v[234:235], v101 src0_sel:WORD_1
	v_cvt_pk_f32_fp8_e32 v[236:237], v109
	v_cvt_pk_f32_fp8_sdwa v[238:239], v109 src0_sel:WORD_1
	v_lshlrev_b32_e32 v212, 16, v122
	v_and_b32_e32 v213, 0xffff0000, v122
	v_lshlrev_b32_e32 v214, 16, v123
	v_and_b32_e32 v215, 0xffff0000, v123
	v_pk_fma_f32 v[212:213], v[232:233], v[240:241], v[212:213] op_sel_hi:[1,0,1]
	v_pk_fma_f32 v[214:215], v[234:235], v[240:241], v[214:215] op_sel_hi:[1,0,1]
	v_pk_fma_f32 v[212:213], v[236:237], v[242:243], v[212:213] op_sel_hi:[1,0,1]
	v_pk_fma_f32 v[214:215], v[238:239], v[242:243], v[214:215] op_sel_hi:[1,0,1]
	v_cvt_pk_f32_fp8_e32 v[224:225], v102
	v_cvt_pk_f32_fp8_sdwa v[226:227], v102 src0_sel:WORD_1
	v_cvt_pk_f32_fp8_e32 v[228:229], v110
	v_cvt_pk_f32_fp8_sdwa v[230:231], v110 src0_sel:WORD_1
	v_lshlrev_b32_e32 v216, 16, v124
	v_and_b32_e32 v217, 0xffff0000, v124
	v_lshlrev_b32_e32 v218, 16, v125
	v_and_b32_e32 v219, 0xffff0000, v125
	v_pk_fma_f32 v[216:217], v[224:225], v[240:241], v[216:217] op_sel_hi:[1,0,1]
	v_pk_fma_f32 v[218:219], v[226:227], v[240:241], v[218:219] op_sel_hi:[1,0,1]
	v_pk_fma_f32 v[216:217], v[228:229], v[242:243], v[216:217] op_sel_hi:[1,0,1]
	v_pk_fma_f32 v[218:219], v[230:231], v[242:243], v[218:219] op_sel_hi:[1,0,1]
	v_cvt_pk_f32_fp8_e32 v[232:233], v103
	v_cvt_pk_f32_fp8_sdwa v[234:235], v103 src0_sel:WORD_1
	v_cvt_pk_f32_fp8_e32 v[236:237], v111
	v_cvt_pk_f32_fp8_sdwa v[238:239], v111 src0_sel:WORD_1
	v_lshlrev_b32_e32 v220, 16, v126
	v_and_b32_e32 v221, 0xffff0000, v126
	v_lshlrev_b32_e32 v222, 16, v127
	v_and_b32_e32 v223, 0xffff0000, v127
	v_pk_fma_f32 v[220:221], v[232:233], v[240:241], v[220:221] op_sel_hi:[1,0,1]
	v_pk_fma_f32 v[222:223], v[234:235], v[240:241], v[222:223] op_sel_hi:[1,0,1]
	v_pk_fma_f32 v[220:221], v[236:237], v[242:243], v[220:221] op_sel_hi:[1,0,1]
	v_pk_fma_f32 v[222:223], v[238:239], v[242:243], v[222:223] op_sel_hi:[1,0,1]
	s_waitcnt vmcnt(55)
	s_add_u32 s56, s64, 0x7000000
	s_addc_u32 s57, s65, 0
	s_add_u32 s58, s56, 0x1000
	s_addc_u32 s59, s57, 0
	global_store_dwordx4 v4, v[192:195], s[56:57] nt
	global_store_dwordx4 v4, v[196:199], s[56:57] offset:1024 nt
	global_store_dwordx4 v4, v[200:203], s[56:57] offset:2048 nt
	global_store_dwordx4 v4, v[204:207], s[56:57] offset:3072 nt
	global_store_dwordx4 v4, v[208:211], s[58:59] nt
	global_store_dwordx4 v4, v[212:215], s[58:59] offset:1024 nt
	global_store_dwordx4 v4, v[216:219], s[58:59] offset:2048 nt
	global_store_dwordx4 v4, v[220:223], s[58:59] offset:3072 nt
